# speedup vs baseline: 1.0153x; 1.0028x over previous
.LBB1_8:
	s_or_b64 exec, exec, s[4:5]
	s_waitcnt vmcnt(1)
	v_mov_b32_e32 v184, 1
	v_lshl_add_u32 v180, v176, 2, v172
	v_lshl_add_u32 v181, v177, 2, v172
	v_lshl_add_u32 v182, v178, 2, v172
	v_lshl_add_u32 v183, v179, 2, v172
	s_waitcnt lgkmcnt(0)
	ds_add_u32 v180, v184
	ds_add_u32 v181, v184
	ds_add_u32 v182, v184
	ds_add_u32 v183, v184
	s_waitcnt lgkmcnt(0)
	ds_read_b32 v151, v173
	s_waitcnt lgkmcnt(0)
	v_cvt_f32_i32_e32 v185, v151
	ds_write_b32 v173, v185 offset:256
	v_add_u32_e32 v10, v172, v2
	s_waitcnt vmcnt(1) lgkmcnt(0)
	s_barrier
	s_nop 0
	ds_read_b128 v[18:21], v10 offset:256
	ds_read_b128 v[22:25], v10 offset:288
	ds_read_b128 v[82:85], v10 offset:320
	ds_read_b128 v[86:89], v10 offset:352
	ds_read_b128 v[74:77], v10 offset:384
	ds_read_b128 v[78:81], v10 offset:416
	ds_read_b128 v[2:5], v213 offset:32768
	ds_read_b128 v[6:9], v213 offset:0
	ds_read_b128 v[66:69], v10 offset:448
	ds_read_b128 v[70:73], v10 offset:480
	ds_read_b128 v[10:13], v213 offset:1024
	s_waitcnt lgkmcnt(3)
	v_pk_mul_f32 v[26:27], v[8:9], v[20:21]
	v_pk_mul_f32 v[28:29], v[6:7], v[18:19]
	ds_read_b128 v[14:17], v213 offset:8192
	s_waitcnt lgkmcnt(1)
	v_pk_mul_f32 v[12:13], v[12:13], v[24:25]
	v_pk_mul_f32 v[10:11], v[10:11], v[22:23]
	v_pk_fma_f32 v[30:31], v[8:9], v[20:21], v[12:13]
	v_pk_fma_f32 v[32:33], v[6:7], v[18:19], v[10:11]
	v_cvt_pk_bf16_f32 v9, v12, v13
	v_cvt_pk_bf16_f32 v7, v26, v27
	v_cvt_pk_bf16_f32 v8, v10, v11
	v_cvt_pk_bf16_f32 v6, v28, v29
	ds_read_b128 v[10:13], v213 offset:33792
	s_nop 0
	v_mfma_f32_32x32x16_bf16 v[34:49], v[2:5], v[6:9], 0
	ds_read_b128 v[6:9], v213 offset:9216
	s_waitcnt lgkmcnt(2)
	v_mul_f32_e32 v26, v16, v20
	v_mul_f32_e32 v27, v17, v21
	v_pk_mul_f32 v[50:51], v[14:15], v[18:19]
	s_mov_b32 s4, 0x3727c5ac
	s_waitcnt lgkmcnt(0)
	v_pk_mul_f32 v[8:9], v[8:9], v[24:25]
	v_pk_mul_f32 v[28:29], v[6:7], v[22:23]
	v_pk_fma_f32 v[90:91], v[16:17], v[20:21], v[8:9]
	v_pk_fma_f32 v[92:93], v[14:15], v[18:19], v[28:29]
	ds_read_b128 v[14:17], v213 offset:2048
	v_cvt_pk_bf16_f32 v9, v8, v9
	v_cvt_pk_bf16_f32 v7, v26, v27
	v_cvt_pk_bf16_f32 v8, v28, v29
	ds_read_b128 v[26:29], v213 offset:3072
	v_cvt_pk_bf16_f32 v6, v50, v51
	s_waitcnt lgkmcnt(1)
	v_pk_mul_f32 v[94:95], v[14:15], v[82:83]
	s_mov_b32 s0, 0x3c800000
	v_mfma_f32_32x32x16_bf16 v[50:65], v[2:5], v[6:9], 0
	v_mul_f32_e32 v2, v16, v84
	v_mul_f32_e32 v3, v17, v85
	s_waitcnt lgkmcnt(0)
	v_mul_f32_e32 v4, v28, v88
	v_mul_f32_e32 v5, v29, v89
	v_pk_mul_f32 v[6:7], v[26:27], v[86:87]
	v_pk_fma_f32 v[8:9], v[16:17], v[84:85], v[4:5]
	v_cvt_pk_bf16_f32 v3, v2, v3
	v_pk_fma_f32 v[14:15], v[14:15], v[82:83], v[6:7]
	v_pk_add_f32 v[26:27], v[8:9], v[30:31]
	v_cvt_pk_bf16_f32 v5, v4, v5
	v_cvt_pk_bf16_f32 v4, v6, v7
	ds_read_b128 v[6:9], v213 offset:10240
	v_pk_add_f32 v[28:29], v[14:15], v[32:33]
	ds_read_b128 v[14:17], v213 offset:11264
	v_cvt_pk_bf16_f32 v2, v94, v95
	s_waitcnt lgkmcnt(1)
	v_pk_mul_f32 v[30:31], v[6:7], v[82:83]
	v_mov_b64_e32 v[152:153], s[4:5]
	v_mfma_f32_32x32x16_bf16 v[34:49], v[10:13], v[2:5], v[34:49]
	v_mul_f32_e32 v2, v8, v84
	v_mul_f32_e32 v3, v9, v85
	s_waitcnt lgkmcnt(0)
	v_mul_f32_e32 v4, v16, v88
	v_mul_f32_e32 v5, v17, v89
	v_pk_mul_f32 v[14:15], v[14:15], v[86:87]
	v_pk_fma_f32 v[8:9], v[8:9], v[84:85], v[4:5]
	v_pk_fma_f32 v[6:7], v[6:7], v[82:83], v[14:15]
	v_cvt_pk_bf16_f32 v5, v4, v5
	v_cvt_pk_bf16_f32 v3, v2, v3
	v_cvt_pk_bf16_f32 v4, v14, v15
	v_pk_add_f32 v[32:33], v[8:9], v[90:91]
	v_pk_add_f32 v[90:91], v[6:7], v[92:93]
	ds_read_b128 v[6:9], v213 offset:34816
	ds_read_b128 v[14:17], v213 offset:4096
	v_cvt_pk_bf16_f32 v2, v30, v31
	s_mov_b32 s13, 0
	s_mov_b64 s[6:7], 0
	v_mfma_f32_32x32x16_bf16 v[50:65], v[10:13], v[2:5], v[50:65]
	ds_read_b128 v[2:5], v213 offset:5120
	ds_read_b128 v[10:13], v213 offset:12288
	s_waitcnt lgkmcnt(2)
	v_pk_mul_f32 v[30:31], v[16:17], v[76:77]
	v_pk_mul_f32 v[92:93], v[14:15], v[74:75]
	s_waitcnt lgkmcnt(1)
	v_pk_mul_f32 v[4:5], v[4:5], v[80:81]
	v_pk_mul_f32 v[94:95], v[2:3], v[78:79]
	v_pk_fma_f32 v[2:3], v[16:17], v[76:77], v[4:5]
	v_cvt_pk_bf16_f32 v5, v4, v5
	v_pk_add_f32 v[96:97], v[2:3], v[26:27]
	v_cvt_pk_bf16_f32 v3, v30, v31
	v_cvt_pk_bf16_f32 v4, v94, v95
	v_cvt_pk_bf16_f32 v2, v92, v93
	v_pk_fma_f32 v[14:15], v[14:15], v[74:75], v[94:95]
	s_waitcnt lgkmcnt(0)
	v_pk_mul_f32 v[30:31], v[10:11], v[74:75]
	v_mfma_f32_32x32x16_bf16 v[34:49], v[6:9], v[2:5], v[34:49]
	ds_read_b128 v[2:5], v213 offset:13312
	v_add_f32_e32 v98, v14, v28
	v_add_f32_e32 v99, v15, v29
	ds_read_b128 v[14:17], v213 offset:35840
	v_pk_mul_f32 v[26:27], v[12:13], v[76:77]
	s_waitcnt lgkmcnt(1)
	v_pk_mul_f32 v[4:5], v[4:5], v[80:81]
	v_pk_mul_f32 v[28:29], v[2:3], v[78:79]
	v_pk_fma_f32 v[2:3], v[12:13], v[76:77], v[4:5]
	v_pk_fma_f32 v[10:11], v[10:11], v[74:75], v[28:29]
	v_pk_add_f32 v[32:33], v[2:3], v[32:33]
	v_pk_add_f32 v[92:93], v[10:11], v[90:91]
	ds_read_b128 v[10:13], v213 offset:6144
	v_cvt_pk_bf16_f32 v5, v4, v5
	v_cvt_pk_bf16_f32 v3, v26, v27
	v_cvt_pk_bf16_f32 v4, v28, v29
	ds_read_b128 v[26:29], v213 offset:7168
	v_cvt_pk_bf16_f32 v2, v30, v31
	s_waitcnt lgkmcnt(1)
	v_pk_mul_f32 v[30:31], v[10:11], v[66:67]
	v_mfma_f32_32x32x16_bf16 v[50:65], v[6:9], v[2:5], v[50:65]
	v_mul_f32_e32 v2, v12, v68
	v_mul_f32_e32 v3, v13, v69
	s_waitcnt lgkmcnt(0)
	v_mul_f32_e32 v4, v28, v72
	v_mul_f32_e32 v5, v29, v73
	v_pk_mul_f32 v[6:7], v[26:27], v[70:71]
	v_pk_fma_f32 v[8:9], v[12:13], v[68:69], v[4:5]
	v_cvt_pk_bf16_f32 v3, v2, v3
	v_pk_fma_f32 v[10:11], v[10:11], v[66:67], v[6:7]
	v_pk_add_f32 v[94:95], v[8:9], v[96:97]
	v_cvt_pk_bf16_f32 v5, v4, v5
	v_cvt_pk_bf16_f32 v4, v6, v7
	ds_read_b128 v[6:9], v213 offset:14336
	v_pk_add_f32 v[96:97], v[10:11], v[98:99]
	ds_read_b128 v[10:13], v213 offset:15360
	v_cvt_pk_bf16_f32 v2, v30, v31
	s_waitcnt lgkmcnt(1)
	v_pk_mul_f32 v[30:31], v[6:7], v[66:67]
	v_mfma_f32_32x32x16_bf16 v[34:49], v[14:17], v[2:5], v[34:49]
	s_waitcnt lgkmcnt(0)
	v_mul_f32_e32 v10, v10, v70
	v_mul_f32_e32 v11, v11, v71
	v_mul_f32_e32 v2, v8, v68
	v_mul_f32_e32 v3, v9, v69
	v_pk_mul_f32 v[4:5], v[12:13], v[72:73]
	v_pk_fma_f32 v[6:7], v[6:7], v[66:67], v[10:11]
	v_pk_fma_f32 v[8:9], v[8:9], v[68:69], v[4:5]
	v_pk_add_f32 v[92:93], v[6:7], v[92:93]
	v_cvt_pk_bf16_f32 v3, v2, v3
	v_pk_add_f32 v[90:91], v[8:9], v[32:33]
	v_cvt_pk_bf16_f32 v5, v4, v5
	v_cvt_pk_bf16_f32 v4, v10, v11
	ds_read_b128 v[26:29], v213 offset:36864
	ds_read_b128 v[6:9], v213 offset:16384
	v_cvt_pk_bf16_f32 v2, v30, v31
	ds_read_b128 v[98:101], v213 offset:25600
	ds_read_b128 v[102:105], v213 offset:37888
	v_mfma_f32_32x32x16_bf16 v[50:65], v[14:17], v[2:5], v[50:65]
	ds_read_b128 v[2:5], v213 offset:17408
	ds_read_b128 v[30:33], v213 offset:24576
	s_waitcnt lgkmcnt(4)
	v_pk_mul_f32 v[12:13], v[6:7], v[18:19]
	v_pk_mul_f32 v[10:11], v[8:9], v[20:21]
	s_waitcnt lgkmcnt(1)
	v_pk_mul_f32 v[14:15], v[2:3], v[22:23]
	v_pk_mul_f32 v[22:23], v[98:99], v[22:23]
	v_pk_fma_f32 v[112:113], v[6:7], v[18:19], v[14:15]
	s_waitcnt lgkmcnt(0)
	v_pk_mul_f32 v[114:115], v[30:31], v[18:19]
	v_pk_fma_f32 v[118:119], v[30:31], v[18:19], v[22:23]
	v_pk_mul_f32 v[4:5], v[4:5], v[24:25]
	v_pk_mul_f32 v[106:107], v[32:33], v[20:21]
	v_pk_mul_f32 v[24:25], v[100:101], v[24:25]
	ds_read_b128 v[98:101], v213 offset:18432
	v_cvt_pk_bf16_f32 v19, v106, v107
	ds_read_b128 v[106:109], v213 offset:19456
	v_pk_fma_f32 v[110:111], v[8:9], v[20:21], v[4:5]
	v_cvt_pk_bf16_f32 v5, v4, v5
	v_cvt_pk_bf16_f32 v3, v10, v11
	v_cvt_pk_bf16_f32 v4, v14, v15
	s_waitcnt lgkmcnt(0)
	v_pk_mul_f32 v[106:107], v[106:107], v[86:87]
	v_cvt_pk_bf16_f32 v2, v12, v13
	v_pk_mul_f32 v[120:121], v[98:99], v[82:83]
	v_pk_mul_f32 v[108:109], v[108:109], v[88:89]
	v_pk_fma_f32 v[98:99], v[98:99], v[82:83], v[106:107]
	v_mfma_f32_32x32x16_bf16 v[2:17], v[26:29], v[2:5], 0
	v_cvt_pk_bf16_f32 v18, v114, v115
	v_mul_f32_e32 v114, v100, v84
	v_mul_f32_e32 v115, v101, v85
	v_fma_f32 v100, v100, v84, v108
	v_fma_f32 v101, v101, v85, v109
	v_pk_add_f32 v[124:125], v[98:99], v[112:113]
	v_pk_add_f32 v[122:123], v[100:101], v[110:111]
	v_cvt_pk_bf16_f32 v101, v108, v109
	v_cvt_pk_bf16_f32 v100, v106, v107
	ds_read_b128 v[106:109], v213 offset:26624
	v_pk_fma_f32 v[116:117], v[32:33], v[20:21], v[24:25]
	v_cvt_pk_bf16_f32 v21, v24, v25
	v_cvt_pk_bf16_f32 v20, v22, v23
	ds_read_b128 v[110:113], v213 offset:27648
	v_cvt_pk_bf16_f32 v99, v114, v115
	v_mfma_f32_32x32x16_bf16 v[18:33], v[26:29], v[18:21], 0
	v_cvt_pk_bf16_f32 v98, v120, v121
	s_waitcnt lgkmcnt(1)
	v_mul_f32_e32 v114, v106, v82
	v_mul_f32_e32 v115, v107, v83
	s_waitcnt lgkmcnt(0)
	v_pk_mul_f32 v[86:87], v[110:111], v[86:87]
	v_pk_mul_f32 v[88:89], v[112:113], v[88:89]
	v_pk_fma_f32 v[82:83], v[106:107], v[82:83], v[86:87]
	v_mfma_f32_32x32x16_bf16 v[2:17], v[102:105], v[98:101], v[2:17]
	v_mul_f32_e32 v98, v108, v84
	v_mul_f32_e32 v99, v109, v85
	v_fma_f32 v84, v108, v84, v88
	v_fma_f32 v85, v109, v85, v89
	v_add_f32_e32 v108, v82, v118
	v_add_f32_e32 v109, v83, v119
	v_cvt_pk_bf16_f32 v83, v98, v99
	v_pk_add_f32 v[106:107], v[84:85], v[116:117]
	v_cvt_pk_bf16_f32 v85, v88, v89
	v_cvt_pk_bf16_f32 v84, v86, v87
	ds_read_b128 v[86:89], v213 offset:38912
	ds_read_b128 v[98:101], v213 offset:20480
	v_cvt_pk_bf16_f32 v82, v114, v115
	s_waitcnt lgkmcnt(0)
	v_pk_mul_f32 v[110:111], v[100:101], v[76:77]
	v_mfma_f32_32x32x16_bf16 v[18:33], v[102:105], v[82:85], v[18:33]
	ds_read_b128 v[82:85], v213 offset:21504
	ds_read_b128 v[102:105], v213 offset:28672
	v_mul_f32_e32 v112, v98, v74
	v_mul_f32_e32 v113, v99, v75
	s_waitcnt lgkmcnt(1)
	v_pk_mul_f32 v[84:85], v[84:85], v[80:81]
	v_pk_mul_f32 v[114:115], v[82:83], v[78:79]
	v_pk_fma_f32 v[82:83], v[100:101], v[76:77], v[84:85]
	v_cvt_pk_bf16_f32 v85, v84, v85
	v_pk_add_f32 v[116:117], v[82:83], v[122:123]
	v_cvt_pk_bf16_f32 v83, v110, v111
	v_cvt_pk_bf16_f32 v84, v114, v115
	v_cvt_pk_bf16_f32 v82, v112, v113
	v_pk_fma_f32 v[98:99], v[98:99], v[74:75], v[114:115]
	s_waitcnt lgkmcnt(0)
	v_pk_mul_f32 v[112:113], v[102:103], v[74:75]
	v_mfma_f32_32x32x16_bf16 v[2:17], v[86:89], v[82:85], v[2:17]
	ds_read_b128 v[82:85], v213 offset:29696
	v_add_f32_e32 v118, v98, v124
	v_add_f32_e32 v119, v99, v125
	v_mul_f32_e32 v110, v104, v76
	v_mul_f32_e32 v111, v105, v77
	ds_read_b128 v[98:101], v213 offset:39936
	s_waitcnt lgkmcnt(1)
	v_pk_mul_f32 v[78:79], v[82:83], v[78:79]
	v_pk_mul_f32 v[80:81], v[84:85], v[80:81]
	v_pk_fma_f32 v[74:75], v[102:103], v[74:75], v[78:79]
	v_pk_fma_f32 v[76:77], v[104:105], v[76:77], v[80:81]
	v_pk_add_f32 v[104:105], v[74:75], v[108:109]
	v_pk_add_f32 v[102:103], v[76:77], v[106:107]
	v_cvt_pk_bf16_f32 v77, v80, v81
	v_cvt_pk_bf16_f32 v76, v78, v79
	ds_read_b128 v[78:81], v213 offset:22528
	ds_read_b128 v[82:85], v213 offset:23552
	v_cvt_pk_bf16_f32 v75, v110, v111
	v_cvt_pk_bf16_f32 v74, v112, v113
	s_waitcnt lgkmcnt(0)
	v_pk_mul_f32 v[82:83], v[82:83], v[70:71]
	v_mfma_f32_32x32x16_bf16 v[18:33], v[86:89], v[74:77], v[18:33]
	v_mul_f32_e32 v74, v80, v68
	v_mul_f32_e32 v75, v81, v69
	v_mul_f32_e32 v76, v84, v72
	v_mul_f32_e32 v77, v85, v73
	v_mul_f32_e32 v86, v78, v66
	v_mul_f32_e32 v87, v79, v67
	v_pk_fma_f32 v[80:81], v[80:81], v[68:69], v[76:77]
	v_pk_fma_f32 v[78:79], v[78:79], v[66:67], v[82:83]
	v_cvt_pk_bf16_f32 v75, v74, v75
	v_pk_add_f32 v[88:89], v[80:81], v[116:117]
	v_pk_add_f32 v[106:107], v[78:79], v[118:119]
	ds_read_b128 v[78:81], v213 offset:30720
	v_cvt_pk_bf16_f32 v77, v76, v77
	v_cvt_pk_bf16_f32 v76, v82, v83
	ds_read_b128 v[82:85], v213 offset:31744
	v_cvt_pk_bf16_f32 v74, v86, v87
	s_waitcnt lgkmcnt(0)
	v_pk_mul_f32 v[72:73], v[84:85], v[72:73]
	v_mfma_f32_32x32x16_bf16 v[2:17], v[98:101], v[74:77], v[2:17]
	v_mul_f32_e32 v74, v80, v68
	v_mul_f32_e32 v75, v81, v69
	v_fma_f32 v68, v80, v68, v72
	v_fma_f32 v69, v81, v69, v73
	v_mul_f32_e32 v70, v82, v70
	v_mul_f32_e32 v71, v83, v71
	v_pk_add_f32 v[84:85], v[68:69], v[102:103]
	v_cvt_pk_bf16_f32 v69, v72, v73
	v_pk_mov_b32 v[72:73], v[96:97], v[94:95] op_sel:[1,0]
	v_mov_b32_e32 v97, v95
	v_pk_add_f32 v[72:73], v[72:73], v[96:97]
	v_pk_mul_f32 v[76:77], v[78:79], v[66:67]
	v_pk_fma_f32 v[66:67], v[78:79], v[66:67], v[70:71]
	v_pk_add_f32 v[72:73], v[72:73], v[72:73] op_sel:[0,1] op_sel_hi:[1,0]
	v_pk_add_f32 v[86:87], v[66:67], v[104:105]
	v_mov_b32_e32 v66, v72
	s_nop 1
	v_permlane32_swap_b32_e32 v72, v66
	v_add_f32_e32 v66, v72, v66
	v_cvt_pk_bf16_f32 v67, v74, v75
	v_rcp_f32_e32 v74, v66
	v_cvt_pk_bf16_f32 v68, v70, v71
	v_cvt_pk_bf16_f32 v66, v76, v77
	v_pk_mul_f32 v[70:71], v[46:47], v[74:75] op_sel_hi:[1,0]
	s_nop 0
	v_mfma_f32_32x32x16_bf16 v[18:33], v[98:101], v[66:69], v[18:33]
	v_mul_f32_e32 v66, v42, v74
	v_mul_f32_e32 v67, v43, v74
	v_pk_mov_b32 v[42:43], v[92:93], v[90:91] op_sel:[1,0]
	v_mov_b32_e32 v93, v91
	v_pk_add_f32 v[42:43], v[42:43], v[92:93]
	v_pk_mul_f32 v[68:69], v[44:45], v[74:75] op_sel_hi:[1,0]
	v_pk_add_f32 v[42:43], v[42:43], v[42:43] op_sel:[0,1] op_sel_hi:[1,0]
	v_pk_mov_b32 v[44:45], v[106:107], v[88:89] op_sel:[1,0]
	v_mov_b32_e32 v43, v42
	s_nop 1
	v_permlane32_swap_b32_e32 v42, v43
	v_add_f32_e32 v42, v42, v43
	v_rcp_f32_e32 v42, v42
	v_mov_b32_e32 v107, v89
	v_pk_add_f32 v[44:45], v[44:45], v[106:107]
	v_pk_mul_f32 v[72:73], v[48:49], v[74:75] op_sel_hi:[1,0]
	v_pk_add_f32 v[44:45], v[44:45], v[44:45] op_sel:[0,1] op_sel_hi:[1,0]
	v_pk_mul_f32 v[36:37], v[36:37], v[74:75] op_sel_hi:[1,0]
	v_pk_mul_f32 v[38:39], v[38:39], v[74:75] op_sel_hi:[1,0]
	v_pk_mul_f32 v[40:41], v[40:41], v[74:75] op_sel_hi:[1,0]
	v_pk_mul_f32 v[34:35], v[34:35], v[74:75] op_sel_hi:[1,0]
	v_pk_mul_f32 v[74:75], v[58:59], v[42:43] op_sel_hi:[1,0]
	v_pk_mul_f32 v[78:79], v[60:61], v[42:43] op_sel_hi:[1,0]
	v_pk_mul_f32 v[80:81], v[62:63], v[42:43] op_sel_hi:[1,0]
	v_pk_mul_f32 v[82:83], v[64:65], v[42:43] op_sel_hi:[1,0]
	v_pk_mul_f32 v[92:93], v[52:53], v[42:43] op_sel_hi:[1,0]
	v_mov_b32_e32 v43, v44
	s_nop 1
	v_permlane32_swap_b32_e32 v44, v43
	v_add_f32_e32 v43, v44, v43
	v_rcp_f32_e32 v76, v43
	v_pk_mul_f32 v[96:97], v[54:55], v[42:43] op_sel_hi:[1,0]
	v_pk_mul_f32 v[94:95], v[56:57], v[42:43] op_sel_hi:[1,0]
	v_pk_mul_f32 v[98:99], v[50:51], v[42:43] op_sel_hi:[1,0]
	v_pk_mul_f32 v[100:101], v[4:5], v[76:77] op_sel_hi:[1,0]
	v_pk_mov_b32 v[4:5], v[86:87], v[84:85] op_sel:[1,0]
	v_mov_b32_e32 v87, v85
	v_pk_add_f32 v[4:5], v[4:5], v[86:87]
	v_pk_mul_f32 v[102:103], v[6:7], v[76:77] op_sel_hi:[1,0]
	v_pk_add_f32 v[104:105], v[4:5], v[4:5] op_sel:[0,1] op_sel_hi:[1,0]
	v_cvt_pk_bf16_f32 v7, v40, v41
	s_nop 0
	ds_read_b128 v[84:87], v150 offset:52224
	ds_read_b128 v[50:53], v150 offset:35840
	ds_read_b128 v[54:57], v150 offset:36864
	ds_read_b128 v[58:61], v150 offset:37888
	ds_read_b128 v[62:65], v150 offset:38912
	v_cvt_pk_bf16_f32 v6, v38, v39
	v_cvt_pk_bf16_f32 v5, v36, v37
	v_cvt_pk_bf16_f32 v4, v34, v35
	ds_read_b128 v[88:91], v150 offset:53248
	ds_read_b128 v[34:37], v150 offset:39936
	ds_read_b128 v[38:41], v150 offset:40960
	ds_read_b128 v[42:45], v150 offset:41984
	ds_read_b128 v[46:49], v150 offset:43008
	v_cvt_pk_bf16_f32 v95, v94, v95
	v_cvt_pk_bf16_f32 v94, v96, v97
	v_cvt_pk_bf16_f32 v93, v92, v93
	v_cvt_pk_bf16_f32 v92, v98, v99
	s_waitcnt lgkmcnt(5)
	v_mfma_f32_32x32x16_bf16 v[50:65], v[84:87], v[4:7], v[50:65]
	v_mul_f32_e32 v10, v10, v76
	v_mul_f32_e32 v11, v11, v76
	v_mul_f32_e32 v12, v12, v76
	v_mul_f32_e32 v13, v13, v76
	v_mul_f32_e32 v8, v8, v76
	v_mul_f32_e32 v9, v9, v76
	v_mov_b32_e32 v77, v104
	s_nop 1
	v_permlane32_swap_b32_e32 v104, v77
	v_cvt_pk_bf16_f32 v73, v72, v73
	s_waitcnt lgkmcnt(0)
	v_mfma_f32_32x32x16_bf16 v[34:49], v[84:87], v[92:95], v[34:49]
	v_cvt_pk_bf16_f32 v72, v70, v71
	v_cvt_pk_bf16_f32 v70, v66, v67
	v_add_f32_e32 v66, v104, v77
	v_cvt_pk_bf16_f32 v71, v68, v69
	v_rcp_f32_e32 v104, v66
	v_cvt_pk_bf16_f32 v69, v82, v83
	v_cvt_pk_bf16_f32 v68, v80, v81
	v_cvt_pk_bf16_f32 v67, v78, v79
	v_cvt_pk_bf16_f32 v66, v74, v75
	ds_read_b128 v[78:81], v150 offset:54272
	v_mfma_f32_32x32x16_bf16 v[50:65], v[88:91], v[70:73], v[50:65]
	v_mul_f32_e32 v2, v2, v76
	v_mul_f32_e32 v3, v3, v76
	v_mul_f32_e32 v20, v20, v104
	v_mul_f32_e32 v21, v21, v104
	v_cvt_pk_bf16_f32 v85, v8, v9
	v_cvt_pk_bf16_f32 v82, v2, v3
	v_pk_mul_f32 v[2:3], v[22:23], v[104:105] op_sel_hi:[1,0]
	v_pk_mul_f32 v[8:9], v[24:25], v[104:105] op_sel_hi:[1,0]
	v_pk_mul_f32 v[18:19], v[18:19], v[104:105] op_sel_hi:[1,0]
	v_mfma_f32_32x32x16_bf16 v[34:49], v[88:91], v[66:69], v[34:49]
	v_cvt_pk_bf16_f32 v84, v102, v103
	v_cvt_pk_bf16_f32 v83, v100, v101
	ds_read_b128 v[86:89], v150 offset:55296
	v_cvt_pk_bf16_f32 v99, v8, v9
	v_cvt_pk_bf16_f32 v98, v2, v3
	v_cvt_pk_bf16_f32 v97, v20, v21
	v_cvt_pk_bf16_f32 v96, v18, v19
	s_waitcnt lgkmcnt(1)
	v_mfma_f32_32x32x16_bf16 v[50:65], v[78:81], v[82:85], v[50:65]
	v_mul_f32_e32 v2, v14, v76
	v_mul_f32_e32 v3, v15, v76
	v_mul_f32_e32 v8, v16, v76
	v_mul_f32_e32 v9, v17, v76
	v_mul_f32_e32 v14, v26, v104
	v_mul_f32_e32 v15, v27, v104
	v_cvt_pk_bf16_f32 v77, v8, v9
	v_cvt_pk_bf16_f32 v76, v2, v3
	v_cvt_pk_bf16_f32 v74, v10, v11
	v_pk_mul_f32 v[2:3], v[28:29], v[104:105] op_sel_hi:[1,0]
	v_mfma_f32_32x32x16_bf16 v[34:49], v[78:81], v[96:99], v[34:49]
	v_mul_f32_e32 v8, v30, v104
	v_mul_f32_e32 v9, v31, v104
	v_mul_f32_e32 v10, v32, v104
	v_mul_f32_e32 v11, v33, v104
	v_cvt_pk_bf16_f32 v75, v12, v13
	v_cvt_pk_bf16_f32 v81, v10, v11
	v_cvt_pk_bf16_f32 v80, v8, v9
	v_cvt_pk_bf16_f32 v79, v2, v3
	v_cvt_pk_bf16_f32 v78, v14, v15
	s_waitcnt lgkmcnt(0)
	v_mfma_f32_32x32x16_bf16 v[50:65], v[86:89], v[74:77], v[50:65]
	v_mfma_f32_32x32x16_bf16 v[34:49], v[86:89], v[78:81], v[34:49]
	ds_read_b128 v[86:89], v150 offset:56320
	ds_read_b128 v[18:21], v150 offset:44032
	ds_read_b128 v[22:25], v150 offset:45056
	ds_read_b128 v[26:29], v150 offset:46080
	ds_read_b128 v[30:33], v150 offset:47104
	ds_read_b128 v[100:103], v150 offset:57344
	s_waitcnt lgkmcnt(1)
	v_mfma_f32_32x32x16_bf16 v[18:33], v[86:89], v[4:7], v[18:33]
	ds_read_b128 v[2:5], v150 offset:48128
	ds_read_b128 v[6:9], v150 offset:49152
	ds_read_b128 v[10:13], v150 offset:50176
	ds_read_b128 v[14:17], v150 offset:51200
	s_waitcnt lgkmcnt(0)
	v_mfma_f32_32x32x16_bf16 v[2:17], v[86:89], v[92:95], v[2:17]
	v_mfma_f32_32x32x16_bf16 v[18:33], v[100:103], v[70:73], v[18:33]
	v_mfma_f32_32x32x16_bf16 v[2:17], v[100:103], v[66:69], v[2:17]
	ds_read_b128 v[66:69], v150 offset:58368
	ds_read_b128 v[70:73], v150 offset:59392
	s_waitcnt lgkmcnt(1)
	v_mfma_f32_32x32x16_bf16 v[18:33], v[66:69], v[82:85], v[18:33]
	v_mfma_f32_32x32x16_bf16 v[2:17], v[66:69], v[96:99], v[2:17]
	s_waitcnt lgkmcnt(0)
	v_mfma_f32_32x32x16_bf16 v[18:33], v[70:73], v[74:77], v[18:33]
	v_mfma_f32_32x32x16_bf16 v[2:17], v[70:73], v[78:81], v[2:17]
	s_nop 10
	v_mul_f32_e32 v66, v22, v22
	v_mul_f32_e32 v67, v23, v23
	v_mul_f32_e32 v68, v30, v30
	v_mul_f32_e32 v69, v31, v31
	v_mul_f32_e32 v70, v24, v24
	v_mul_f32_e32 v71, v25, v25
	v_pk_mul_f32 v[72:73], v[32:33], v[32:33]
	v_pk_mul_f32 v[74:75], v[20:21], v[20:21]
	v_pk_mul_f32 v[76:77], v[28:29], v[28:29]
	v_pk_mul_f32 v[78:79], v[26:27], v[26:27]
	v_pk_mul_f32 v[80:81], v[18:19], v[18:19]
	v_pk_fma_f32 v[78:79], v[58:59], v[58:59], v[78:79]
	v_pk_fma_f32 v[76:77], v[60:61], v[60:61], v[76:77]
	v_pk_fma_f32 v[74:75], v[52:53], v[52:53], v[74:75]
	v_pk_fma_f32 v[72:73], v[64:65], v[64:65], v[72:73]
	v_pk_fma_f32 v[70:71], v[56:57], v[56:57], v[70:71]
	v_pk_fma_f32 v[68:69], v[62:63], v[62:63], v[68:69]
	v_pk_fma_f32 v[66:67], v[54:55], v[54:55], v[66:67]
	v_pk_fma_f32 v[80:81], v[50:51], v[50:51], v[80:81]
	v_pk_add_f32 v[66:67], v[66:67], v[68:69]
	v_pk_add_f32 v[68:69], v[70:71], v[72:73]
	v_pk_add_f32 v[70:71], v[74:75], v[76:77]
	v_pk_add_f32 v[72:73], v[80:81], v[78:79]
	v_pk_add_f32 v[68:69], v[70:71], v[68:69]
	v_pk_add_f32 v[66:67], v[72:73], v[66:67]
	v_pk_mul_f32 v[72:73], v[14:15], v[14:15]
	v_pk_mov_b32 v[70:71], v[66:67], v[68:69] op_sel:[1,0]
	v_mov_b32_e32 v67, v69
	v_pk_add_f32 v[66:67], v[70:71], v[66:67]
	v_pk_mul_f32 v[70:71], v[6:7], v[6:7]
	v_pk_mul_f32 v[74:75], v[8:9], v[8:9]
	v_pk_mul_f32 v[76:77], v[16:17], v[16:17]
	v_pk_mul_f32 v[78:79], v[4:5], v[4:5]
	v_pk_mul_f32 v[80:81], v[12:13], v[12:13]
	v_pk_mul_f32 v[82:83], v[10:11], v[10:11]
	v_pk_mul_f32 v[84:85], v[2:3], v[2:3]
	v_pk_fma_f32 v[82:83], v[42:43], v[42:43], v[82:83]
	v_pk_fma_f32 v[80:81], v[44:45], v[44:45], v[80:81]
	v_pk_fma_f32 v[78:79], v[36:37], v[36:37], v[78:79]
	v_pk_fma_f32 v[76:77], v[48:49], v[48:49], v[76:77]
	v_pk_fma_f32 v[74:75], v[40:41], v[40:41], v[74:75]
	v_pk_fma_f32 v[72:73], v[46:47], v[46:47], v[72:73]
	v_pk_fma_f32 v[70:71], v[38:39], v[38:39], v[70:71]
	v_pk_fma_f32 v[84:85], v[34:35], v[34:35], v[84:85]
	v_pk_add_f32 v[70:71], v[70:71], v[72:73]
	v_pk_add_f32 v[72:73], v[74:75], v[76:77]
	v_pk_add_f32 v[74:75], v[78:79], v[80:81]
	v_pk_add_f32 v[76:77], v[84:85], v[82:83]
	v_pk_add_f32 v[72:73], v[74:75], v[72:73]
	v_pk_add_f32 v[70:71], v[76:77], v[70:71]
	v_pk_add_f32 v[66:67], v[66:67], v[66:67] op_sel:[0,1] op_sel_hi:[1,0]
	v_pk_mov_b32 v[74:75], v[70:71], v[72:73] op_sel:[1,0]
	v_mov_b32_e32 v71, v73
	v_pk_add_f32 v[70:71], v[74:75], v[70:71]
	v_mov_b32_e32 v69, v66
	v_pk_add_f32 v[70:71], v[70:71], v[70:71] op_sel:[0,1] op_sel_hi:[1,0]
	s_nop 0
	v_permlane32_swap_b32_e32 v66, v69
	v_mov_b32_e32 v68, v70
	s_nop 1
	v_permlane32_swap_b32_e32 v70, v68
	v_mov_b32_e32 v71, v66
	v_pk_add_f32 v[66:67], v[70:71], v[68:69]
	v_pk_fma_f32 v[66:67], v[66:67], s[0:1], v[152:153] op_sel_hi:[1,0,0]
	s_mov_b32 s1, 0x800000
	v_mul_f32_e32 v68, 0x4b800000, v67
	v_cmp_gt_f32_e32 vcc, s1, v67
	s_nop 1
	v_cndmask_b32_e32 v67, v67, v68, vcc
	v_rsq_f32_e32 v67, v67
	s_nop 0
	v_mul_f32_e32 v68, 0x45800000, v67
	v_cndmask_b32_e32 v68, v67, v68, vcc
	v_pk_mul_f32 v[158:159], v[50:51], v[68:69] op_sel_hi:[1,0]
	v_pk_mul_f32 v[50:51], v[18:19], v[68:69] op_sel_hi:[1,0]
	v_mul_f32_e32 v18, 0x4b800000, v66
	v_cmp_gt_f32_e32 vcc, s1, v66
	v_pk_mul_f32 v[80:81], v[60:61], v[68:69] op_sel_hi:[1,0]
	v_pk_mul_f32 v[60:61], v[28:29], v[68:69] op_sel_hi:[1,0]
	v_cndmask_b32_e32 v18, v66, v18, vcc
	v_rsq_f32_e32 v18, v18
	v_pk_mul_f32 v[78:79], v[58:59], v[68:69] op_sel_hi:[1,0]
	v_pk_mul_f32 v[160:161], v[52:53], v[68:69] op_sel_hi:[1,0]
	v_pk_mul_f32 v[82:83], v[54:55], v[68:69] op_sel_hi:[1,0]
	v_mul_f32_e32 v19, 0x45800000, v18
	v_cndmask_b32_e32 v28, v18, v19, vcc
	v_pk_mul_f32 v[168:169], v[56:57], v[68:69] op_sel_hi:[1,0]
	v_pk_mul_f32 v[58:59], v[26:27], v[68:69] op_sel_hi:[1,0]
	v_pk_mul_f32 v[52:53], v[20:21], v[68:69] op_sel_hi:[1,0]
	v_pk_mul_f32 v[54:55], v[22:23], v[68:69] op_sel_hi:[1,0]
	v_pk_mul_f32 v[56:57], v[24:25], v[68:69] op_sel_hi:[1,0]
	v_pk_mul_f32 v[18:19], v[42:43], v[28:29] op_sel_hi:[1,0]
	v_pk_mul_f32 v[20:21], v[44:45], v[28:29] op_sel_hi:[1,0]
	v_pk_mul_f32 v[22:23], v[46:47], v[28:29] op_sel_hi:[1,0]
	v_pk_mul_f32 v[26:27], v[48:49], v[28:29] op_sel_hi:[1,0]
	v_pk_mul_f32 v[162:163], v[34:35], v[28:29] op_sel_hi:[1,0]
	v_pk_mul_f32 v[164:165], v[36:37], v[28:29] op_sel_hi:[1,0]
	v_pk_mul_f32 v[166:167], v[38:39], v[28:29] op_sel_hi:[1,0]
	v_pk_mul_f32 v[24:25], v[40:41], v[28:29] op_sel_hi:[1,0]
	v_pk_mul_f32 v[104:105], v[2:3], v[28:29] op_sel_hi:[1,0]
	v_pk_mul_f32 v[112:113], v[4:5], v[28:29] op_sel_hi:[1,0]
	ds_read_b128 v[2:5], v150 offset:60416
	ds_read_b128 v[34:37], v174 offset:32768
	ds_read_b128 v[38:41], v174 offset:32800
	ds_read_b128 v[42:45], v174 offset:32832
	ds_read_b128 v[46:49], v174 offset:32864
	v_cvt_pk_bf16_f32 v129, v168, v169
	v_cvt_pk_bf16_f32 v128, v82, v83
	v_cvt_pk_bf16_f32 v127, v160, v161
	v_cvt_pk_bf16_f32 v126, v158, v159
	v_cvt_pk_bf16_f32 v137, v24, v25
	v_cvt_pk_bf16_f32 v136, v166, v167
	v_cvt_pk_bf16_f32 v135, v164, v165
	s_waitcnt lgkmcnt(0)
	v_mfma_f32_32x32x16_bf16 v[86:101], v[2:5], v[126:129], v[34:49]
	v_cvt_pk_bf16_f32 v134, v162, v163
	v_mul_f32_e32 v84, v62, v68
	v_mul_f32_e32 v85, v63, v68
	v_mul_f32_e32 v170, v64, v68
	v_mul_f32_e32 v171, v65, v68
	v_pk_mul_f32 v[62:63], v[30:31], v[68:69] op_sel_hi:[1,0]
	v_pk_mul_f32 v[64:65], v[32:33], v[68:69] op_sel_hi:[1,0]
	v_pk_mul_f32 v[116:117], v[6:7], v[28:29] op_sel_hi:[1,0]
	v_pk_mul_f32 v[154:155], v[8:9], v[28:29] op_sel_hi:[1,0]
	v_mfma_f32_32x32x16_bf16 v[34:49], v[2:5], v[134:137], v[34:49]
	ds_read_b128 v[6:9], v150 offset:61440
	ds_read_b128 v[66:69], v174 offset:32896
	ds_read_b128 v[106:109], v150 offset:64512
	v_cvt_pk_bf16_f32 v125, v170, v171
	v_cvt_pk_bf16_f32 v124, v84, v85
	v_cvt_pk_bf16_f32 v123, v80, v81
	v_cvt_pk_bf16_f32 v122, v78, v79
	v_cvt_pk_bf16_f32 v149, v26, v27
	v_cvt_pk_bf16_f32 v148, v22, v23
	v_cvt_pk_bf16_f32 v147, v20, v21
	v_cvt_pk_bf16_f32 v146, v18, v19
	s_waitcnt lgkmcnt(2)
	v_mfma_f32_32x32x16_bf16 v[86:101], v[6:9], v[122:125], v[86:101]
	v_mul_f32_e32 v102, v10, v28
	v_mul_f32_e32 v103, v11, v28
	v_mul_f32_e32 v110, v12, v28
	v_mul_f32_e32 v111, v13, v28
	v_mul_f32_e32 v114, v14, v28
	v_mul_f32_e32 v115, v15, v28
	v_pk_mul_f32 v[156:157], v[16:17], v[28:29] op_sel_hi:[1,0]
	ds_read_b128 v[176:179], v174 offset:33536
	ds_read_b128 v[180:183], v174 offset:33568
	ds_read_b128 v[184:187], v174 offset:33600
	ds_read_b128 v[28:31], v174 offset:33632
	ds_read_b128 v[188:191], v174 offset:33792
	ds_read_b128 v[192:195], v174 offset:33824
	ds_read_b128 v[196:199], v174 offset:33856
	ds_read_b128 v[200:203], v174 offset:33888
	ds_read_b128 v[204:207], v150 offset:62464
	v_cvt_pk_bf16_f32 v133, v56, v57
	v_mfma_f32_32x32x16_bf16 v[34:49], v[6:9], v[146:149], v[34:49]
	v_cvt_pk_bf16_f32 v132, v54, v55
	v_cvt_pk_bf16_f32 v131, v52, v53
	v_cvt_pk_bf16_f32 v130, v50, v51
	ds_read_b128 v[70:73], v174 offset:33664
	ds_read_b128 v[74:77], v174 offset:33920
	ds_read_b128 v[208:211], v150 offset:63488
	v_cvt_pk_bf16_f32 v145, v154, v155
	v_cvt_pk_bf16_f32 v144, v116, v117
	v_cvt_pk_bf16_f32 v143, v112, v113
	v_cvt_pk_bf16_f32 v142, v104, v105
	s_waitcnt lgkmcnt(3)
	v_mfma_f32_32x32x16_bf16 v[86:101], v[204:207], v[130:133], v[86:101]
	v_cvt_pk_bf16_f32 v121, v64, v65
	v_cvt_pk_bf16_f32 v120, v62, v63
	v_cvt_pk_bf16_f32 v119, v60, v61
	v_cvt_pk_bf16_f32 v118, v58, v59
	v_cvt_pk_bf16_f32 v141, v156, v157
	v_cvt_pk_bf16_f32 v140, v114, v115
	v_cvt_pk_bf16_f32 v139, v110, v111
	v_mfma_f32_32x32x16_bf16 v[34:49], v[204:207], v[142:145], v[34:49]
	v_cvt_pk_bf16_f32 v138, v102, v103
	v_fma_f32 v16, v30, v170, v202
	v_fma_f32 v17, v31, v171, v203
	v_fma_f32 v14, v28, v84, v200
	v_fma_f32 v15, v29, v85, v201
	v_pk_fma_f32 v[12:13], v[186:187], v[80:81], v[198:199]
	v_pk_fma_f32 v[10:11], v[184:185], v[78:79], v[196:197]
	v_pk_fma_f32 v[8:9], v[182:183], v[168:169], v[194:195]
	s_waitcnt lgkmcnt(0)
	v_mfma_f32_32x32x16_bf16 v[86:101], v[208:211], v[118:121], v[86:101]
	v_fma_f32 v6, v180, v82, v192
	v_fma_f32 v7, v181, v83, v193
	ds_read_b128 v[78:81], v174 offset:33760
	ds_read_b128 v[82:85], v174 offset:33248
	v_fma_f32 v4, v178, v160, v190
	v_fma_f32 v5, v179, v161, v191
	v_pk_fma_f32 v[2:3], v[176:177], v[158:159], v[188:189]
	v_pk_fma_f32 v[32:33], v[30:31], v[26:27], v[202:203]
	v_pk_fma_f32 v[30:31], v[28:29], v[22:23], v[200:201]
	v_pk_fma_f32 v[28:29], v[186:187], v[20:21], v[198:199]
	v_pk_fma_f32 v[26:27], v[184:185], v[18:19], v[196:197]
	v_pk_fma_f32 v[24:25], v[182:183], v[24:25], v[194:195]
	v_pk_fma_f32 v[22:23], v[180:181], v[166:167], v[192:193]
	v_pk_fma_f32 v[20:21], v[178:179], v[164:165], v[190:191]
	v_pk_fma_f32 v[18:19], v[176:177], v[162:163], v[188:189]
	ds_read_b128 v[158:161], v174 offset:33696
	ds_read_b128 v[162:165], v174 offset:33728
	ds_read_b128 v[166:169], v174 offset:33952
	ds_read_b128 v[176:179], v174 offset:33984
	ds_read_b128 v[180:183], v174 offset:34016
	ds_read_b128 v[184:187], v212 offset:11264
	v_mfma_f32_32x32x16_bf16 v[34:49], v[208:211], v[138:141], v[34:49]
	v_cvt_pk_bf16_f32 v86, v86, v87
	v_cvt_pk_bf16_f32 v87, v88, v89
	v_cvt_pk_bf16_f32 v88, v90, v91
	v_cvt_pk_bf16_f32 v89, v92, v93
	ds_read_b128 v[90:93], v212 offset:12288
	v_pk_max_i16 v86, v86, 0
	v_pk_max_i16 v87, v87, 0
	v_pk_max_i16 v88, v88, 0
	v_pk_max_i16 v89, v89, 0
	s_nop 1
	s_nop 0
	v_cvt_pk_bf16_f32 v188, v34, v35
	v_cvt_pk_bf16_f32 v189, v36, v37
	v_cvt_pk_bf16_f32 v190, v38, v39
	v_cvt_pk_bf16_f32 v191, v40, v41
	s_waitcnt lgkmcnt(1)
	v_mfma_f32_32x32x16_bf16 v[2:17], v[184:187], v[86:89], v[2:17]
	v_pk_max_i16 v188, v188, 0
	v_pk_max_i16 v189, v189, 0
	v_pk_max_i16 v190, v190, 0
	v_pk_max_i16 v191, v191, 0
	v_cvt_pk_bf16_f32 v94, v94, v95
	v_cvt_pk_bf16_f32 v95, v96, v97
	v_cvt_pk_bf16_f32 v96, v98, v99
	v_cvt_pk_bf16_f32 v97, v100, v101
	v_cvt_pk_bf16_f32 v98, v42, v43
	v_cvt_pk_bf16_f32 v99, v44, v45
	v_mfma_f32_32x32x16_bf16 v[18:33], v[184:187], v[188:191], v[18:33]
	ds_read_b128 v[184:187], v212 offset:19456
	v_cvt_pk_bf16_f32 v100, v46, v47
	v_cvt_pk_bf16_f32 v101, v48, v49
	v_fma_f32 v64, v80, v64, v182
	v_fma_f32 v65, v81, v65, v183
	v_pk_fma_f32 v[62:63], v[78:79], v[62:63], v[180:181]
	v_pk_fma_f32 v[60:61], v[164:165], v[60:61], v[178:179]
	v_pk_fma_f32 v[58:59], v[162:163], v[58:59], v[176:177]
	v_pk_max_i16 v94, v94, 0
	v_pk_max_i16 v95, v95, 0
	v_pk_max_i16 v96, v96, 0
	v_pk_max_i16 v97, v97, 0
	v_pk_max_i16 v98, v98, 0
	v_pk_max_i16 v99, v99, 0
	v_pk_max_i16 v100, v100, 0
	v_pk_max_i16 v101, v101, 0
	v_pk_fma_f32 v[56:57], v[160:161], v[56:57], v[168:169]
	s_waitcnt lgkmcnt(1)
	v_mfma_f32_32x32x16_bf16 v[2:17], v[90:93], v[94:97], v[2:17]
	v_fma_f32 v54, v158, v54, v166
	v_fma_f32 v55, v159, v55, v167
	v_fma_f32 v52, v72, v52, v76
	v_fma_f32 v53, v73, v53, v77
	v_fma_f32 v50, v70, v50, v74
	v_fma_f32 v51, v71, v51, v75
	v_pk_fma_f32 v[48:49], v[80:81], v[156:157], v[182:183]
	v_pk_fma_f32 v[46:47], v[78:79], v[114:115], v[180:181]
	v_pk_fma_f32 v[44:45], v[164:165], v[110:111], v[178:179]
	v_pk_fma_f32 v[42:43], v[162:163], v[102:103], v[176:177]
	v_mfma_f32_32x32x16_bf16 v[18:33], v[90:93], v[98:101], v[18:33]
	ds_read_b128 v[90:93], v212 offset:20480
	v_fma_f32 v40, v160, v154, v168
	v_fma_f32 v41, v161, v155, v169
	v_fma_f32 v38, v158, v116, v166
	v_fma_f32 v39, v159, v117, v167
	v_pk_fma_f32 v[36:37], v[72:73], v[112:113], v[76:77]
	v_pk_fma_f32 v[34:35], v[70:71], v[104:105], v[74:75]
	s_waitcnt lgkmcnt(1)
	v_mfma_f32_32x32x16_bf16 v[50:65], v[184:187], v[86:89], v[50:65]
	ds_read_b128 v[70:73], v174 offset:32928
	ds_read_b128 v[74:77], v174 offset:32960
	ds_read_b128 v[78:81], v174 offset:32992
	ds_read_b128 v[86:89], v174 offset:33024
	ds_read_b128 v[110:113], v212 offset:1024
	v_mfma_f32_32x32x16_bf16 v[34:49], v[184:187], v[188:191], v[34:49]
	s_waitcnt lgkmcnt(5)
	v_mfma_f32_32x32x16_bf16 v[50:65], v[90:93], v[94:97], v[50:65]
	v_mfma_f32_32x32x16_bf16 v[34:49], v[90:93], v[98:101], v[34:49]
	s_waitcnt lgkmcnt(2)
	v_mfma_f32_32x32x16_bf16 v[90:105], v[106:109], v[126:129], v[66:81]
	v_mfma_f32_32x32x16_bf16 v[66:81], v[106:109], v[134:137], v[66:81]
	ds_read_b128 v[106:109], v212 offset:0
	s_waitcnt lgkmcnt(0)
	v_mfma_f32_32x32x16_bf16 v[90:105], v[106:109], v[122:125], v[90:105]
	v_mfma_f32_32x32x16_bf16 v[66:81], v[106:109], v[146:149], v[66:81]
	ds_read_b128 v[106:109], v212 offset:2048
	v_mfma_f32_32x32x16_bf16 v[90:105], v[110:113], v[130:133], v[90:105]
	v_mfma_f32_32x32x16_bf16 v[66:81], v[110:113], v[142:145], v[66:81]
	ds_read_b128 v[110:113], v212 offset:13312
	s_waitcnt lgkmcnt(1)
	v_mfma_f32_32x32x16_bf16 v[90:105], v[106:109], v[118:121], v[90:105]
	v_mfma_f32_32x32x16_bf16 v[66:81], v[106:109], v[138:141], v[66:81]
	s_nop 10
	v_cvt_pk_bf16_f32 v90, v90, v91
	v_cvt_pk_bf16_f32 v91, v92, v93
	v_cvt_pk_bf16_f32 v92, v94, v95
	v_cvt_pk_bf16_f32 v94, v98, v99
	v_cvt_pk_bf16_f32 v95, v100, v101
	ds_read_b128 v[98:101], v212 offset:21504
	v_cvt_pk_bf16_f32 v66, v66, v67
	v_cvt_pk_bf16_f32 v67, v68, v69
	v_cvt_pk_bf16_f32 v68, v70, v71
	v_cvt_pk_bf16_f32 v93, v96, v97
	v_cvt_pk_bf16_f32 v69, v72, v73
	ds_read_b128 v[70:73], v212 offset:14336
	v_pk_max_i16 v90, v90, 0
	v_pk_max_i16 v91, v91, 0
	v_pk_max_i16 v92, v92, 0
	v_pk_max_i16 v93, v93, 0
	v_pk_max_i16 v66, v66, 0
	v_pk_max_i16 v67, v67, 0
	v_pk_max_i16 v68, v68, 0
	v_pk_max_i16 v69, v69, 0
	v_cvt_pk_bf16_f32 v96, v102, v103
	s_waitcnt lgkmcnt(2)
	v_mfma_f32_32x32x16_bf16 v[2:17], v[110:113], v[90:93], v[2:17]
	v_cvt_pk_bf16_f32 v97, v104, v105
	v_cvt_pk_bf16_f32 v74, v74, v75
	v_cvt_pk_bf16_f32 v75, v76, v77
	v_cvt_pk_bf16_f32 v76, v78, v79
	v_cvt_pk_bf16_f32 v77, v80, v81
	v_pk_max_i16 v94, v94, 0
	v_pk_max_i16 v95, v95, 0
	v_pk_max_i16 v96, v96, 0
	v_pk_max_i16 v97, v97, 0
	v_pk_max_i16 v74, v74, 0
	v_pk_max_i16 v75, v75, 0
	v_pk_max_i16 v76, v76, 0
	v_pk_max_i16 v77, v77, 0
	v_mfma_f32_32x32x16_bf16 v[18:33], v[110:113], v[66:69], v[18:33]
	s_waitcnt lgkmcnt(1)
	v_mfma_f32_32x32x16_bf16 v[34:49], v[98:101], v[66:69], v[34:49]
	ds_read_b128 v[66:69], v212 offset:22528
	v_mfma_f32_32x32x16_bf16 v[50:65], v[98:101], v[90:93], v[50:65]
	s_waitcnt lgkmcnt(1)
	v_mfma_f32_32x32x16_bf16 v[2:17], v[70:73], v[94:97], v[2:17]
	v_mfma_f32_32x32x16_bf16 v[18:33], v[70:73], v[74:77], v[18:33]
	ds_read_b128 v[78:81], v212 offset:3072
	s_waitcnt lgkmcnt(1)
	v_mfma_f32_32x32x16_bf16 v[50:65], v[66:69], v[94:97], v[50:65]
	ds_read_b128 v[90:93], v174 offset:33056
	ds_read_b128 v[94:97], v174 offset:33088
	ds_read_b128 v[98:101], v174 offset:33120
	ds_read_b128 v[70:73], v174 offset:33152
	v_mfma_f32_32x32x16_bf16 v[34:49], v[66:69], v[74:77], v[34:49]
	ds_read_b128 v[66:69], v212 offset:4096
	ds_read_b128 v[74:77], v212 offset:5120
	s_waitcnt lgkmcnt(3)
	v_mfma_f32_32x32x16_bf16 v[102:117], v[78:81], v[126:129], v[86:101]
	v_mfma_f32_32x32x16_bf16 v[86:101], v[78:81], v[134:137], v[86:101]
	s_waitcnt lgkmcnt(1)
	v_mfma_f32_32x32x16_bf16 v[86:101], v[66:69], v[146:149], v[86:101]
	v_mfma_f32_32x32x16_bf16 v[102:117], v[66:69], v[122:125], v[102:117]
	ds_read_b128 v[66:69], v212 offset:6144
	s_waitcnt lgkmcnt(1)
	v_mfma_f32_32x32x16_bf16 v[86:101], v[74:77], v[142:145], v[86:101]
	v_mfma_f32_32x32x16_bf16 v[102:117], v[74:77], v[130:133], v[102:117]
	ds_read_b128 v[74:77], v212 offset:15360
	s_waitcnt lgkmcnt(1)
	v_mfma_f32_32x32x16_bf16 v[86:101], v[66:69], v[138:141], v[86:101]
	v_mfma_f32_32x32x16_bf16 v[102:117], v[66:69], v[118:121], v[102:117]
	s_nop 10
	v_cvt_pk_bf16_f32 v78, v86, v87
	v_cvt_pk_bf16_f32 v80, v90, v91
	v_cvt_pk_bf16_f32 v79, v88, v89
	v_cvt_pk_bf16_f32 v81, v92, v93
	ds_read_b128 v[86:89], v212 offset:16384
	ds_read_b128 v[90:93], v212 offset:23552
	v_cvt_pk_bf16_f32 v66, v102, v103
	v_cvt_pk_bf16_f32 v67, v104, v105
	v_cvt_pk_bf16_f32 v68, v106, v107
	v_cvt_pk_bf16_f32 v69, v108, v109
	v_pk_max_i16 v66, v66, 0
	v_pk_max_i16 v67, v67, 0
	v_pk_max_i16 v68, v68, 0
	v_pk_max_i16 v69, v69, 0
	v_pk_max_i16 v78, v78, 0
	v_pk_max_i16 v79, v79, 0
	v_pk_max_i16 v80, v80, 0
	v_pk_max_i16 v81, v81, 0
	v_cvt_pk_bf16_f32 v94, v94, v95
	s_waitcnt lgkmcnt(2)
	v_mfma_f32_32x32x16_bf16 v[18:33], v[74:77], v[78:81], v[18:33]
	v_cvt_pk_bf16_f32 v95, v96, v97
	v_cvt_pk_bf16_f32 v96, v98, v99
	v_cvt_pk_bf16_f32 v97, v100, v101
	v_pk_max_i16 v94, v94, 0
	v_pk_max_i16 v95, v95, 0
	v_pk_max_i16 v96, v96, 0
	v_pk_max_i16 v97, v97, 0
	v_mfma_f32_32x32x16_bf16 v[2:17], v[74:77], v[66:69], v[2:17]
	v_cvt_pk_bf16_f32 v74, v110, v111
	v_cvt_pk_bf16_f32 v75, v112, v113
	v_cvt_pk_bf16_f32 v76, v114, v115
	v_cvt_pk_bf16_f32 v77, v116, v117
	v_pk_max_i16 v74, v74, 0
	v_pk_max_i16 v75, v75, 0
	v_pk_max_i16 v76, v76, 0
	v_pk_max_i16 v77, v77, 0
	s_waitcnt lgkmcnt(0)
	v_mfma_f32_32x32x16_bf16 v[50:65], v[90:93], v[66:69], v[50:65]
	ds_read_b128 v[66:69], v212 offset:24576
	v_mfma_f32_32x32x16_bf16 v[34:49], v[90:93], v[78:81], v[34:49]
	ds_read_b128 v[102:105], v212 offset:7168
	v_mfma_f32_32x32x16_bf16 v[2:17], v[86:89], v[74:77], v[2:17]
	s_waitcnt lgkmcnt(1)
	v_mfma_f32_32x32x16_bf16 v[50:65], v[66:69], v[74:77], v[50:65]
	ds_read_b128 v[74:77], v174 offset:33184
	ds_read_b128 v[78:81], v174 offset:33216
	v_mfma_f32_32x32x16_bf16 v[34:49], v[66:69], v[94:97], v[34:49]
	ds_read_b128 v[66:69], v212 offset:8192
	v_mfma_f32_32x32x16_bf16 v[18:33], v[86:89], v[94:97], v[18:33]
	s_waitcnt lgkmcnt(1)
	v_mfma_f32_32x32x16_bf16 v[86:101], v[102:105], v[126:129], v[70:85]
	v_mfma_f32_32x32x16_bf16 v[70:85], v[102:105], v[134:137], v[70:85]
	ds_read_b128 v[102:105], v212 offset:9216
	v_lshlrev_b32_e32 v135, 2, v1
	v_add_u32_e32 v134, v172, v174
	s_waitcnt lgkmcnt(1)
	v_mfma_f32_32x32x16_bf16 v[86:101], v[66:69], v[122:125], v[86:101]
	v_mfma_f32_32x32x16_bf16 v[70:85], v[66:69], v[146:149], v[70:85]
	ds_read_b128 v[66:69], v212 offset:10240
	s_waitcnt lgkmcnt(1)
	v_mfma_f32_32x32x16_bf16 v[86:101], v[102:105], v[130:133], v[86:101]
	v_mfma_f32_32x32x16_bf16 v[70:85], v[102:105], v[142:145], v[70:85]
	ds_read_b128 v[102:105], v212 offset:17408
	s_waitcnt lgkmcnt(1)
	v_mfma_f32_32x32x16_bf16 v[86:101], v[66:69], v[118:121], v[86:101]
	v_mfma_f32_32x32x16_bf16 v[70:85], v[66:69], v[138:141], v[70:85]
	s_nop 10
	v_cvt_pk_bf16_f32 v68, v90, v91
	v_cvt_pk_bf16_f32 v69, v92, v93
	ds_read_b128 v[90:93], v212 offset:25600
	v_cvt_pk_bf16_f32 v66, v86, v87
	v_cvt_pk_bf16_f32 v67, v88, v89
	v_pk_max_i16 v66, v66, 0
	v_pk_max_i16 v67, v67, 0
	v_pk_max_i16 v68, v68, 0
	v_pk_max_i16 v69, v69, 0
	v_cvt_pk_bf16_f32 v70, v70, v71
	v_cvt_pk_bf16_f32 v71, v72, v73
	s_waitcnt lgkmcnt(1)
	v_mfma_f32_32x32x16_bf16 v[2:17], v[102:105], v[66:69], v[2:17]
	v_cvt_pk_bf16_f32 v72, v74, v75
	v_cvt_pk_bf16_f32 v73, v76, v77
	ds_read_b128 v[74:77], v212 offset:18432
	v_cvt_pk_bf16_f32 v86, v94, v95
	v_cvt_pk_bf16_f32 v87, v96, v97
	v_cvt_pk_bf16_f32 v88, v98, v99
	s_waitcnt lgkmcnt(1)
	v_mfma_f32_32x32x16_bf16 v[50:65], v[90:93], v[66:69], v[50:65]
	ds_read_b128 v[66:69], v212 offset:26624
	v_cvt_pk_bf16_f32 v89, v100, v101
	v_pk_max_i16 v86, v86, 0
	v_pk_max_i16 v87, v87, 0
	v_pk_max_i16 v88, v88, 0
	v_pk_max_i16 v89, v89, 0
	v_pk_max_i16 v70, v70, 0
	v_pk_max_i16 v71, v71, 0
	v_pk_max_i16 v72, v72, 0
	v_pk_max_i16 v73, v73, 0
	v_cvt_pk_bf16_f32 v78, v78, v79
	v_cvt_pk_bf16_f32 v79, v80, v81
	s_waitcnt lgkmcnt(1)
	v_mfma_f32_32x32x16_bf16 v[2:17], v[74:77], v[86:89], v[2:17]
	v_cvt_pk_bf16_f32 v80, v82, v83
	v_cvt_pk_bf16_f32 v81, v84, v85
	v_pk_max_i16 v78, v78, 0
	v_pk_max_i16 v79, v79, 0
	v_pk_max_i16 v80, v80, 0
	v_pk_max_i16 v81, v81, 0
	s_waitcnt lgkmcnt(0)
	v_mfma_f32_32x32x16_bf16 v[50:65], v[66:69], v[86:89], v[50:65]
	v_mfma_f32_32x32x16_bf16 v[34:49], v[90:93], v[70:73], v[34:49]
	s_nop 10
	v_add_f32_e32 v130, v10, v58
	v_add_f32_e32 v131, v11, v59
	v_add_f32_e32 v132, v12, v60
	v_add_f32_e32 v133, v13, v61
	v_add_f32_e32 v138, v4, v52
	v_add_f32_e32 v139, v5, v53
	v_pk_add_f32 v[140:141], v[16:17], v[64:65]
	v_pk_add_f32 v[142:143], v[8:9], v[56:57]
	v_pk_add_f32 v[144:145], v[14:15], v[62:63]
	v_pk_add_f32 v[146:147], v[6:7], v[54:55]
	v_mfma_f32_32x32x16_bf16 v[18:33], v[102:105], v[70:73], v[18:33]
	ds_read2st64_b32 v[70:71], v135 offset0:133 offset1:134
	v_add_f32_e32 v148, v2, v50
	v_add_f32_e32 v149, v3, v51
	v_add_f32_e32 v144, v146, v144
	v_add_f32_e32 v145, v147, v145
	v_pk_add_f32 v[140:141], v[142:143], v[140:141]
	v_pk_add_f32 v[132:133], v[138:139], v[132:133]
	v_pk_add_f32 v[130:131], v[148:149], v[130:131]
	v_pk_add_f32 v[132:133], v[132:133], v[140:141]
	v_pk_add_f32 v[130:131], v[130:131], v[144:145]
	v_mfma_f32_32x32x16_bf16 v[34:49], v[66:69], v[78:81], v[34:49]
	v_pk_mov_b32 v[138:139], v[130:131], v[132:133] op_sel:[1,0]
	v_mov_b32_e32 v131, v133
	s_waitcnt vmcnt(0) lgkmcnt(0)
	v_mul_f32_e32 v66, v175, v70
	v_pk_add_f32 v[130:131], v[138:139], v[130:131]
	ds_write_b32 v173, v66 offset:512
	v_mul_f32_e32 v66, v175, v71
	v_pk_add_f32 v[130:131], v[130:131], v[130:131] op_sel:[0,1] op_sel_hi:[1,0]
	s_waitcnt lgkmcnt(0)
	ds_read_b128 v[102:105], v174 offset:34560
	ds_read_b128 v[98:101], v174 offset:34592
	ds_read_b128 v[110:113], v174 offset:34624
	ds_read_b128 v[106:109], v174 offset:34656
	ds_read_b128 v[114:117], v174 offset:34688
	ds_read_b128 v[122:125], v174 offset:34720
	ds_read_b128 v[118:121], v174 offset:34752
	ds_read_b128 v[126:129], v174 offset:34784
	v_mov_b32_dpp v66, v66 quad_perm:[1,0,3,2] row_mask:0xf bank_mask:0xf bound_ctrl:1
	v_mov_b32_e32 v131, v130
	v_fmac_f32_e32 v66, v175, v71
	s_nop 0
	v_permlane32_swap_b32_e32 v130, v131
	v_add_f32_dpp v66, v66, v66 quad_perm:[2,3,0,1] row_mask:0xf bank_mask:0xf bound_ctrl:1
	v_add_f32_e32 v130, v130, v131
	v_fmamk_f32 v65, v130, 0xbc800000, v65
	v_add_f32_dpp v66, v66, v66 row_half_mirror row_mask:0xf bank_mask:0xf bound_ctrl:1
	v_fmamk_f32 v64, v130, 0xbc800000, v64
	v_fmamk_f32 v63, v130, 0xbc800000, v63
	v_fmamk_f32 v62, v130, 0xbc800000, v62
	v_fmamk_f32 v61, v130, 0xbc800000, v61
	v_fmamk_f32 v60, v130, 0xbc800000, v60
	v_fmamk_f32 v59, v130, 0xbc800000, v59
	v_fmamk_f32 v58, v130, 0xbc800000, v58
	v_fmamk_f32 v57, v130, 0xbc800000, v57
	v_fmamk_f32 v56, v130, 0xbc800000, v56
	v_fmamk_f32 v55, v130, 0xbc800000, v55
	v_fmamk_f32 v54, v130, 0xbc800000, v54
	v_fmamk_f32 v53, v130, 0xbc800000, v53
	v_fmamk_f32 v52, v130, 0xbc800000, v52
	v_fmamk_f32 v51, v130, 0xbc800000, v51
	v_fmac_f32_e32 v50, 0xbc800000, v130
	v_add_f32_dpp v66, v66, v66 row_ror:8 row_mask:0xf bank_mask:0xf bound_ctrl:1
	v_fmamk_f32 v17, v130, 0xbc800000, v17
	v_fmamk_f32 v16, v130, 0xbc800000, v16
	v_fmamk_f32 v15, v130, 0xbc800000, v15
	v_fmamk_f32 v14, v130, 0xbc800000, v14
	v_fmamk_f32 v13, v130, 0xbc800000, v13
	v_fmamk_f32 v12, v130, 0xbc800000, v12
	v_fmamk_f32 v11, v130, 0xbc800000, v11
	v_fmamk_f32 v10, v130, 0xbc800000, v10
	v_fmamk_f32 v9, v130, 0xbc800000, v9
	v_fmamk_f32 v8, v130, 0xbc800000, v8
	v_fmamk_f32 v7, v130, 0xbc800000, v7
	v_fmamk_f32 v6, v130, 0xbc800000, v6
	v_fmamk_f32 v5, v130, 0xbc800000, v5
	v_fmamk_f32 v4, v130, 0xbc800000, v4
	v_fmamk_f32 v3, v130, 0xbc800000, v3
	v_fmac_f32_e32 v2, 0xbc800000, v130
	v_pk_mul_f32 v[130:131], v[54:55], v[54:55]
	v_pk_mul_f32 v[132:133], v[62:63], v[62:63]
	v_pk_mul_f32 v[138:139], v[50:51], v[50:51]
	v_pk_mul_f32 v[140:141], v[58:59], v[58:59]
	v_pk_mul_f32 v[142:143], v[56:57], v[56:57]
	v_pk_mul_f32 v[144:145], v[64:65], v[64:65]
	v_pk_mul_f32 v[146:147], v[52:53], v[52:53]
	v_pk_mul_f32 v[148:149], v[60:61], v[60:61]
	v_mov_b32_e32 v67, v66
	v_pk_fma_f32 v[148:149], v[12:13], v[12:13], v[148:149]
	v_pk_fma_f32 v[146:147], v[4:5], v[4:5], v[146:147]
	v_pk_fma_f32 v[144:145], v[16:17], v[16:17], v[144:145]
	v_pk_fma_f32 v[142:143], v[8:9], v[8:9], v[142:143]
	v_pk_fma_f32 v[140:141], v[10:11], v[10:11], v[140:141]
	v_pk_fma_f32 v[138:139], v[2:3], v[2:3], v[138:139]
	v_pk_fma_f32 v[132:133], v[14:15], v[14:15], v[132:133]
	v_pk_fma_f32 v[130:131], v[6:7], v[6:7], v[130:131]
	v_permlane16_swap_b32_e32 v66, v67
	v_pk_add_f32 v[130:131], v[130:131], v[132:133]
	v_pk_add_f32 v[132:133], v[138:139], v[140:141]
	v_pk_add_f32 v[138:139], v[142:143], v[144:145]
	v_pk_add_f32 v[140:141], v[146:147], v[148:149]
	v_mfma_f32_32x32x16_bf16 v[18:33], v[74:77], v[78:81], v[18:33]
	v_add_f32_e32 v136, v66, v67
	ds_read_b128 v[70:73], v134 offset:512
	ds_read_b128 v[66:69], v134 offset:544
	ds_read_b128 v[78:81], v134 offset:576
	ds_read_b128 v[74:77], v134 offset:608
	ds_read_b128 v[82:85], v134 offset:640
	ds_read_b128 v[90:93], v134 offset:672
	ds_read_b128 v[86:89], v134 offset:704
	ds_read_b128 v[94:97], v134 offset:736
	v_pk_add_f32 v[138:139], v[140:141], v[138:139]
	v_pk_add_f32 v[130:131], v[132:133], v[130:131]
	s_waitcnt lgkmcnt(8)
	v_pk_mul_f32 v[140:141], v[126:127], v[62:63]
	v_pk_mov_b32 v[132:133], v[130:131], v[138:139] op_sel:[1,0]
	v_mov_b32_e32 v131, v139
	v_pk_mul_f32 v[138:139], v[122:123], v[54:55]
	v_pk_mul_f32 v[142:143], v[114:115], v[50:51]
	v_pk_mul_f32 v[144:145], v[118:119], v[58:59]
	v_pk_mul_f32 v[146:147], v[124:125], v[56:57]
	v_pk_mul_f32 v[148:149], v[128:129], v[64:65]
	v_pk_mul_f32 v[154:155], v[116:117], v[52:53]
	v_pk_mul_f32 v[156:157], v[120:121], v[60:61]
	v_pk_fma_f32 v[154:155], v[104:105], v[4:5], v[154:155]
	v_pk_fma_f32 v[156:157], v[112:113], v[12:13], v[156:157]
	v_pk_fma_f32 v[148:149], v[108:109], v[16:17], v[148:149]
	v_pk_fma_f32 v[146:147], v[100:101], v[8:9], v[146:147]
	v_pk_fma_f32 v[144:145], v[110:111], v[10:11], v[144:145]
	v_pk_fma_f32 v[142:143], v[102:103], v[2:3], v[142:143]
	v_pk_fma_f32 v[140:141], v[106:107], v[14:15], v[140:141]
	v_pk_fma_f32 v[138:139], v[98:99], v[6:7], v[138:139]
	v_pk_add_f32 v[130:131], v[132:133], v[130:131]
	v_pk_add_f32 v[138:139], v[138:139], v[140:141]
	v_pk_add_f32 v[140:141], v[142:143], v[144:145]
	v_pk_add_f32 v[142:143], v[146:147], v[148:149]
	v_pk_add_f32 v[144:145], v[154:155], v[156:157]
	v_pk_add_f32 v[132:133], v[130:131], v[130:131] op_sel:[0,1] op_sel_hi:[1,0]
	v_pk_add_f32 v[142:143], v[144:145], v[142:143]
	v_pk_add_f32 v[138:139], v[140:141], v[138:139]
	v_add_f32_e32 v133, v142, v143
	v_add_f32_e32 v130, v138, v139
	s_waitcnt lgkmcnt(2)
	v_pk_mul_f32 v[138:139], v[90:91], v[54:55]
	s_waitcnt lgkmcnt(0)
	v_pk_mul_f32 v[140:141], v[94:95], v[62:63]
	v_pk_mul_f32 v[142:143], v[82:83], v[50:51]
	v_pk_mul_f32 v[144:145], v[86:87], v[58:59]
	v_pk_mul_f32 v[146:147], v[92:93], v[56:57]
	v_pk_mul_f32 v[148:149], v[96:97], v[64:65]
	v_pk_mul_f32 v[154:155], v[84:85], v[52:53]
	v_pk_mul_f32 v[156:157], v[88:89], v[60:61]
	v_add_f32_e32 v130, v130, v133
	v_pk_fma_f32 v[156:157], v[80:81], v[12:13], v[156:157]
	v_pk_fma_f32 v[154:155], v[72:73], v[4:5], v[154:155]
	v_pk_fma_f32 v[148:149], v[76:77], v[16:17], v[148:149]
	v_pk_fma_f32 v[146:147], v[68:69], v[8:9], v[146:147]
	v_pk_fma_f32 v[144:145], v[78:79], v[10:11], v[144:145]
	v_pk_fma_f32 v[142:143], v[70:71], v[2:3], v[142:143]
	v_pk_fma_f32 v[140:141], v[74:75], v[14:15], v[140:141]
	v_pk_fma_f32 v[138:139], v[66:67], v[6:7], v[138:139]
	v_mov_b32_e32 v133, v130
	v_pk_add_f32 v[138:139], v[138:139], v[140:141]
	v_pk_add_f32 v[140:141], v[142:143], v[144:145]
	v_pk_add_f32 v[142:143], v[146:147], v[148:149]
	v_pk_add_f32 v[144:145], v[154:155], v[156:157]
	v_permlane32_swap_b32_e32 v130, v133
	v_pk_add_f32 v[142:143], v[144:145], v[142:143]
	v_add_f32_e32 v160, v130, v133
	v_pk_add_f32 v[138:139], v[140:141], v[138:139]
	v_add_f32_e32 v133, v142, v143
	v_pk_add_f32 v[140:141], v[26:27], v[42:43]
	v_pk_add_f32 v[142:143], v[28:29], v[44:45]
	v_pk_add_f32 v[144:145], v[20:21], v[36:37]
	v_pk_add_f32 v[146:147], v[32:33], v[48:49]
	v_pk_add_f32 v[148:149], v[24:25], v[40:41]
	v_pk_add_f32 v[154:155], v[30:31], v[46:47]
	v_pk_add_f32 v[156:157], v[22:23], v[38:39]
	v_pk_add_f32 v[158:159], v[18:19], v[34:35]
	v_pk_add_f32 v[154:155], v[156:157], v[154:155]
	v_pk_add_f32 v[146:147], v[148:149], v[146:147]
	v_pk_add_f32 v[142:143], v[144:145], v[142:143]
	v_pk_add_f32 v[140:141], v[158:159], v[140:141]
	v_pk_add_f32 v[142:143], v[142:143], v[146:147]
	v_pk_add_f32 v[140:141], v[140:141], v[154:155]
	v_add_f32_e32 v130, v138, v139
	v_pk_mov_b32 v[144:145], v[140:141], v[142:143] op_sel:[1,0]
	v_mov_b32_e32 v141, v143
	v_pk_add_f32 v[140:141], v[144:145], v[140:141]
	v_add_f32_e32 v133, v130, v133
	v_pk_add_f32 v[140:141], v[140:141], v[140:141] op_sel:[0,1] op_sel_hi:[1,0]
	v_mov_b32_e32 v131, v132
	v_mov_b32_e32 v130, v140
	s_nop 1
	v_permlane32_swap_b32_e32 v140, v130
	v_add_f32_e32 v130, v140, v130
	v_fmamk_f32 v49, v130, 0xbc800000, v49
	v_fmamk_f32 v48, v130, 0xbc800000, v48
	v_fmamk_f32 v47, v130, 0xbc800000, v47
	v_fmamk_f32 v46, v130, 0xbc800000, v46
	v_fmamk_f32 v45, v130, 0xbc800000, v45
	v_fmamk_f32 v44, v130, 0xbc800000, v44
	v_fmamk_f32 v43, v130, 0xbc800000, v43
	v_fmamk_f32 v42, v130, 0xbc800000, v42
	v_fmamk_f32 v41, v130, 0xbc800000, v41
	v_fmamk_f32 v40, v130, 0xbc800000, v40
	v_fmamk_f32 v39, v130, 0xbc800000, v39
	v_fmamk_f32 v38, v130, 0xbc800000, v38
	v_fmamk_f32 v37, v130, 0xbc800000, v37
	v_fmamk_f32 v36, v130, 0xbc800000, v36
	v_fmamk_f32 v35, v130, 0xbc800000, v35
	v_fmac_f32_e32 v34, 0xbc800000, v130
	v_fmamk_f32 v33, v130, 0xbc800000, v33
	v_fmamk_f32 v32, v130, 0xbc800000, v32
	v_fmamk_f32 v31, v130, 0xbc800000, v31
	v_fmamk_f32 v30, v130, 0xbc800000, v30
	v_fmamk_f32 v29, v130, 0xbc800000, v29
	v_fmamk_f32 v28, v130, 0xbc800000, v28
	v_fmamk_f32 v27, v130, 0xbc800000, v27
	v_fmamk_f32 v26, v130, 0xbc800000, v26
	v_fmamk_f32 v25, v130, 0xbc800000, v25
	v_fmamk_f32 v24, v130, 0xbc800000, v24
	v_fmamk_f32 v23, v130, 0xbc800000, v23
	v_fmamk_f32 v22, v130, 0xbc800000, v22
	v_fmamk_f32 v21, v130, 0xbc800000, v21
	v_fmamk_f32 v20, v130, 0xbc800000, v20
	v_fmamk_f32 v19, v130, 0xbc800000, v19
	v_fmac_f32_e32 v18, 0xbc800000, v130
	v_pk_mul_f32 v[140:141], v[38:39], v[38:39]
	v_pk_mul_f32 v[142:143], v[46:47], v[46:47]
	v_pk_mul_f32 v[144:145], v[34:35], v[34:35]
	v_pk_mul_f32 v[146:147], v[42:43], v[42:43]
	v_pk_mul_f32 v[148:149], v[40:41], v[40:41]
	v_pk_mul_f32 v[154:155], v[48:49], v[48:49]
	v_pk_mul_f32 v[156:157], v[36:37], v[36:37]
	v_pk_mul_f32 v[158:159], v[44:45], v[44:45]
	v_pk_fma_f32 v[156:157], v[20:21], v[20:21], v[156:157]
	v_pk_fma_f32 v[158:159], v[28:29], v[28:29], v[158:159]
	v_pk_fma_f32 v[154:155], v[32:33], v[32:33], v[154:155]
	v_pk_fma_f32 v[148:149], v[24:25], v[24:25], v[148:149]
	v_pk_fma_f32 v[146:147], v[26:27], v[26:27], v[146:147]
	v_pk_fma_f32 v[144:145], v[18:19], v[18:19], v[144:145]
	v_pk_fma_f32 v[142:143], v[30:31], v[30:31], v[142:143]
	v_pk_fma_f32 v[140:141], v[22:23], v[22:23], v[140:141]
	v_permlane32_swap_b32_e32 v132, v131
	v_pk_add_f32 v[140:141], v[140:141], v[142:143]
	v_pk_add_f32 v[142:143], v[144:145], v[146:147]
	v_pk_add_f32 v[144:145], v[148:149], v[154:155]
	v_pk_add_f32 v[146:147], v[156:157], v[158:159]
	v_pk_add_f32 v[140:141], v[142:143], v[140:141]
	v_pk_add_f32 v[144:145], v[146:147], v[144:145]
	v_pk_mul_f32 v[122:123], v[122:123], v[38:39]
	v_pk_mov_b32 v[142:143], v[140:141], v[144:145] op_sel:[1,0]
	v_mov_b32_e32 v141, v145
	v_pk_add_f32 v[140:141], v[142:143], v[140:141]
	v_pk_mul_f32 v[126:127], v[126:127], v[46:47]
	v_pk_add_f32 v[140:141], v[140:141], v[140:141] op_sel:[0,1] op_sel_hi:[1,0]
	v_pk_mul_f32 v[114:115], v[114:115], v[34:35]
	v_mov_b32_e32 v130, v140
	s_nop 1
	v_permlane32_swap_b32_e32 v140, v130
	v_mov_b32_e32 v141, v132
	v_pk_add_f32 v[130:131], v[140:141], v[130:131]
	v_pk_mul_f32 v[118:119], v[118:119], v[42:43]
	v_pk_fma_f32 v[130:131], v[130:131], s[0:1], v[152:153] op_sel_hi:[1,0,0]
	v_pk_mul_f32 v[124:125], v[124:125], v[40:41]
	v_mul_f32_e32 v132, 0x4b800000, v131
	v_cmp_gt_f32_e32 vcc, s1, v131
	v_pk_mul_f32 v[128:129], v[128:129], v[48:49]
	v_pk_mul_f32 v[116:117], v[116:117], v[36:37]
	v_pk_mul_f32 v[120:121], v[120:121], v[44:45]
	v_cndmask_b32_e32 v131, v131, v132, vcc
	v_mul_f32_e32 v132, 0x4b800000, v130
	v_cmp_gt_f32_e64 s[0:1], s1, v130
	v_pk_fma_f32 v[112:113], v[112:113], v[28:29], v[120:121]
	v_pk_fma_f32 v[104:105], v[104:105], v[20:21], v[116:117]
	v_pk_fma_f32 v[108:109], v[108:109], v[32:33], v[128:129]
	v_pk_fma_f32 v[100:101], v[100:101], v[24:25], v[124:125]
	v_pk_fma_f32 v[110:111], v[110:111], v[26:27], v[118:119]
	v_pk_fma_f32 v[102:103], v[102:103], v[18:19], v[114:115]
	v_pk_fma_f32 v[106:107], v[106:107], v[30:31], v[126:127]
	v_pk_fma_f32 v[98:99], v[98:99], v[22:23], v[122:123]
	v_rsq_f32_e32 v131, v131
	v_cndmask_b32_e64 v130, v130, v132, s[0:1]
	v_pk_add_f32 v[98:99], v[98:99], v[106:107]
	v_pk_add_f32 v[102:103], v[102:103], v[110:111]
	v_pk_add_f32 v[100:101], v[100:101], v[108:109]
	v_pk_add_f32 v[104:105], v[104:105], v[112:113]
	v_rsq_f32_e32 v132, v130
	v_pk_add_f32 v[100:101], v[104:105], v[100:101]
	v_pk_add_f32 v[98:99], v[102:103], v[98:99]
	v_mul_f32_e32 v130, 0x45800000, v131
	v_add_f32_e32 v98, v98, v99
	v_add_f32_e32 v99, v100, v101
	v_add_f32_e32 v98, v98, v99
	v_mov_b32_e32 v99, v98
	v_pk_mul_f32 v[90:91], v[90:91], v[38:39]
	v_pk_mul_f32 v[94:95], v[94:95], v[46:47]
	v_pk_mul_f32 v[82:83], v[82:83], v[34:35]
	v_pk_mul_f32 v[86:87], v[86:87], v[42:43]
	v_cndmask_b32_e32 v130, v131, v130, vcc
	v_mul_f32_e32 v131, 0x45800000, v132
	v_permlane32_swap_b32_e32 v98, v99
	v_pk_fma_f32 v[78:79], v[78:79], v[26:27], v[86:87]
	v_pk_fma_f32 v[70:71], v[70:71], v[18:19], v[82:83]
	v_pk_fma_f32 v[74:75], v[74:75], v[30:31], v[94:95]
	v_pk_fma_f32 v[66:67], v[66:67], v[22:23], v[90:91]
	v_cndmask_b32_e64 v131, v132, v131, s[0:1]
	v_add_f32_e32 v98, v98, v99
	v_pk_add_f32 v[66:67], v[66:67], v[74:75]
	v_pk_add_f32 v[70:71], v[70:71], v[78:79]
	v_mul_f32_e32 v139, v160, v130
	v_mul_f32_e32 v98, v98, v131
	v_pk_add_f32 v[66:67], v[70:71], v[66:67]
	v_cmp_gt_u32_e32 vcc, 32, v1
	v_add_f32_e32 v66, v66, v67
	v_pk_mul_f32 v[92:93], v[92:93], v[40:41]
	v_cndmask_b32_e32 v67, v98, v139, vcc
	v_add_f32_e32 v67, s12, v67
	v_pk_mul_f32 v[96:97], v[96:97], v[48:49]
	v_pk_mul_f32 v[84:85], v[84:85], v[36:37]
	v_pk_mul_f32 v[88:89], v[88:89], v[44:45]
	v_mul_f32_e32 v67, 0xbfb8aa3b, v67
	v_pk_fma_f32 v[80:81], v[80:81], v[28:29], v[88:89]
	v_pk_fma_f32 v[72:73], v[72:73], v[20:21], v[84:85]
	v_pk_fma_f32 v[76:77], v[76:77], v[32:33], v[96:97]
	v_pk_fma_f32 v[68:69], v[68:69], v[24:25], v[92:93]
	v_exp_f32_e32 v70, v67
	v_pk_add_f32 v[68:69], v[68:69], v[76:77]
	v_pk_add_f32 v[72:73], v[72:73], v[80:81]
	v_cmp_lt_i32_e64 s[0:1], 0, v151
	v_pk_add_f32 v[68:69], v[72:73], v[68:69]
	v_mov_b32_e32 v137, v136
	v_add_f32_e32 v67, v68, v69
	v_add_f32_e32 v67, v66, v67
	v_add_f32_e32 v66, 1.0, v70
	v_rcp_f32_e32 v66, v66
	v_mov_b32_e32 v69, 0xff800000
	v_mov_b32_e32 v138, v133
	v_mov_b32_e32 v68, v67
	v_cndmask_b32_e64 v70, v69, v66, s[0:1]
	v_mbcnt_lo_u32_b32 v66, -1, 0
	v_mbcnt_hi_u32_b32 v66, -1, v66
	v_permlane32_swap_b32_e32 v136, v137
	v_permlane32_swap_b32_e32 v133, v138
	v_permlane32_swap_b32_e32 v67, v68
	v_and_b32_e32 v86, 64, v66
	s_mov_b32 s14, 8
	s_mov_b32 s13, 0
	v_mov_b32_e32 v66, 0
	s_waitcnt lgkmcnt(0)
